# attention: K/V ring LDS-DMA issue moved from behind the step barrier to the end of the step (on v11)
# speedup vs baseline: 1.0071x; 1.0003x over previous
; #define ATT_DMAK(tile, slot) do { _Pragma("unroll") for (int i = 0; i < 4; ++i) { const int pc = (wv + 8 * i) < 25 ? (wv + 8 * i) : 24; \
;         __builtin_amdgcn_global_load_lds((const unsigned*)((const char*)Kbh + (size_t)(tile) * (64 * 384) + doffK[i]), (LAS unsigned*)(lds + (slot) * KT_BYTES + pc * 1024), 16, 0, 0); } } while (0)
; #define ATT_DMAV(tile, slot) do { _Pragma("unroll") for (int i = 0; i < 3; ++i) { const int pc = (wv + 8 * i) < 18 ? (wv + 8 * i) : 17; \
;         __builtin_amdgcn_global_load_lds((const unsigned*)((const char*)Vbh + (size_t)(tile) * 128 + doffV[i]), (LAS unsigned*)(lds + VRING + (slot) * VT_BYTES + pc * 1024), 16, 0, 0); } } while (0)
; __device__ __forceinline__ void attn_unit(const bf16_t* Qrows  , const bf16_t* Kbh, const bf16_t* Vbh, int nkeys, bf16_t* Orows, LAS unsigned char* lds) {
;     ...
;         if (j + 4 < nt) ATT_DMAK(j + 4, v0);
;         if (j + 3 < nt) ATT_DMAV(j + 3, v0 == 0 ? 2 : v0 - 1);
.LBB0_1235:
	s_add_i32 s15, s14, 1
	s_cmp_lg_u32 s14, 2
	s_cselect_b32 s14, s15, 0
	s_mul_i32 s15, s14, 0x6400
	v_add_u32_e32 v70, s15, v185
	ds_read_b128 v[66:69], v70
	ds_read_b128 v[166:169], v70 offset:32
	ds_read_b128 v[170:173], v70 offset:64
	ds_read_b128 v[188:191], v70 offset:96
	ds_read_b128 v[192:195], v70 offset:128
	ds_read_b128 v[196:199], v70 offset:160
	ds_read_b128 v[200:203], v70 offset:192
	ds_read_b128 v[216:219], v70 offset:224
	ds_read_b128 v[220:223], v70 offset:256
	ds_read_b128 v[224:227], v70 offset:288
	ds_read_b128 v[228:231], v70 offset:320
	ds_read_b128 v[146:149], v70 offset:352
	s_waitcnt lgkmcnt(11)
	v_mfma_f32_32x32x16_bf16 v[66:81], v[66:69], v[142:145], 0
	v_sub_f32_e32 v82, v82, v183
	v_exp_f32_e32 v82, v82
	v_sub_f32_e32 v94, v94, v183
	v_exp_f32_e32 v94, v94
	v_add_f32_e32 v165, 0, v82
	v_add_f32_e32 v165, v94, v165
	s_waitcnt lgkmcnt(10)
	v_mfma_f32_32x32x16_bf16 v[66:81], v[166:169], v[138:141], v[66:81]
	v_sub_f32_e32 v83, v83, v183
	v_exp_f32_e32 v83, v83
	v_sub_f32_e32 v95, v95, v183
	v_exp_f32_e32 v95, v95
	v_add_f32_e32 v165, v83, v165
	v_cvt_pk_bf16_f32 v82, v82, v83
	v_add_f32_e32 v165, v95, v165
	v_sub_f32_e32 v83, v84, v183
	s_waitcnt lgkmcnt(9)
	v_mfma_f32_32x32x16_bf16 v[66:81], v[170:173], v[134:137], v[66:81]
	v_exp_f32_e32 v83, v83
	v_sub_f32_e32 v96, v96, v183
	v_add_f32_e32 v84, v83, v165
	v_exp_f32_e32 v165, v96
	s_nop 0
	v_add_f32_e32 v84, v165, v84
	s_waitcnt lgkmcnt(8)
	v_mfma_f32_32x32x16_bf16 v[66:81], v[188:191], v[130:133], v[66:81]
	v_sub_f32_e32 v85, v85, v183
	v_exp_f32_e32 v85, v85
	v_sub_f32_e32 v96, v97, v183
	v_exp_f32_e32 v97, v96
	v_cvt_pk_bf16_f32 v96, v94, v95
	v_add_f32_e32 v84, v85, v84
	v_cvt_pk_bf16_f32 v83, v83, v85
	v_add_f32_e32 v84, v97, v84
	v_cvt_pk_bf16_f32 v97, v165, v97
	s_waitcnt lgkmcnt(7)
	v_mfma_f32_32x32x16_bf16 v[66:81], v[192:195], v[126:129], v[66:81]
	v_sub_f32_e32 v85, v86, v183
	v_exp_f32_e32 v85, v85
	s_nop 0
	v_add_f32_e32 v84, v85, v84
	s_waitcnt lgkmcnt(6)
	v_mfma_f32_32x32x16_bf16 v[66:81], v[196:199], v[122:125], v[66:81]
	v_sub_f32_e32 v86, v87, v183
	v_exp_f32_e32 v86, v86
	s_nop 0
	v_add_f32_e32 v87, v86, v84
	v_cvt_pk_bf16_f32 v84, v85, v86
	s_waitcnt lgkmcnt(5)
	v_mfma_f32_32x32x16_bf16 v[66:81], v[200:203], v[118:121], v[66:81]
	v_sub_f32_e32 v85, v88, v183
	v_exp_f32_e32 v85, v85
	s_nop 0
	v_add_f32_e32 v86, v85, v87
	s_waitcnt lgkmcnt(4)
	v_mfma_f32_32x32x16_bf16 v[66:81], v[216:219], v[114:117], v[66:81]
	v_sub_f32_e32 v87, v89, v183
	v_exp_f32_e32 v87, v87
	s_nop 0
	v_add_f32_e32 v86, v87, v86
	v_cvt_pk_bf16_f32 v85, v85, v87
	v_sub_f32_e32 v87, v90, v183
	v_exp_f32_e32 v90, v87
	s_waitcnt lgkmcnt(3)
	v_mfma_f32_32x32x16_bf16 v[66:81], v[220:223], v[110:113], v[66:81]
	v_add_u32_e32 v165, s13, v187
	v_add_f32_e32 v94, v90, v86
	ds_read_b128 v[86:89], v165
	ds_read_b128 v[166:169], v165 offset:32
	s_waitcnt lgkmcnt(4)
	v_mfma_f32_32x32x16_bf16 v[66:81], v[224:227], v[106:109], v[66:81]
	v_sub_f32_e32 v91, v91, v183
	ds_read_b128 v[170:173], v165 offset:4608
	ds_read_b128 v[188:191], v165 offset:4640
	v_exp_f32_e32 v91, v91
	s_nop 0
	v_add_f32_e32 v95, v91, v94
	v_cvt_pk_bf16_f32 v94, v90, v91
	s_waitcnt lgkmcnt(5)
	v_mfma_f32_32x32x16_bf16 v[66:81], v[228:231], v[102:105], v[66:81]
	v_sub_f32_e32 v90, v92, v183
	ds_read_b128 v[192:195], v165 offset:9216
	ds_read_b128 v[196:199], v165 offset:9248
	v_exp_f32_e32 v90, v90
	s_nop 0
	v_add_f32_e32 v91, v90, v95
	v_sub_f32_e32 v92, v93, v183
	v_exp_f32_e32 v92, v92
	s_waitcnt lgkmcnt(6)
	v_mfma_f32_32x32x16_bf16 v[66:81], v[146:149], v[98:101], v[66:81]
	v_add_f32_e32 v186, v92, v91
	v_cvt_pk_bf16_f32 v95, v90, v92
	ds_read_b128 v[90:93], v165 offset:13824
	ds_read_b128 v[146:149], v165 offset:13856
	s_waitcnt lgkmcnt(0)
	v_mfma_f32_32x32x16_bf16 v[50:65], v[86:89], v[82:85], v[50:65]
	v_add_f32_e32 v186, v164, v186
	v_mfma_f32_32x32x16_bf16 v[34:49], v[170:173], v[82:85], v[34:49]
	v_mfma_f32_32x32x16_bf16 v[18:33], v[192:195], v[82:85], v[18:33]
	v_mfma_f32_32x32x16_bf16 v[2:17], v[90:93], v[82:85], v[2:17]
	v_mfma_f32_32x32x16_bf16 v[50:65], v[166:169], v[94:97], v[50:65]
	v_mfma_f32_32x32x16_bf16 v[34:49], v[188:191], v[94:97], v[34:49]
	v_mfma_f32_32x32x16_bf16 v[18:33], v[196:199], v[94:97], v[18:33]
	v_mfma_f32_32x32x16_bf16 v[2:17], v[146:149], v[94:97], v[2:17]
	s_and_b64 vcc, exec, s[0:1]
	s_cbranch_vccnz .LattB_v
	s_mul_i32 s13, s12, 0x6400
	s_add_i32 s13, s13, 0
	s_add_u32 s16, s80, s2
	s_addc_u32 s17, s81, s3
	s_add_u32 s16, s16, 0x30e90000
	s_addc_u32 s17, s17, 0
	s_add_i32 m0, s13, s65
	s_nop 0
	global_load_lds_dwordx4 v208, s[16:17]
	s_add_i32 m0, s13, s66
	s_nop 0
	global_load_lds_dwordx4 v209, s[16:17]
	s_add_i32 m0, s13, s67
	s_add_i32 s13, s13, s68
	global_load_lds_dwordx4 v210, s[16:17]
	s_add_i32 m0, s13, 0x6000
	s_nop 0
	global_load_lds_dwordx4 v211, s[16:17]

; #define ATT_DMAK(tile, slot) do { _Pragma("unroll") for (int i = 0; i < 4; ++i) { const int pc = (wv + 8 * i) < 25 ? (wv + 8 * i) : 24; \
;         __builtin_amdgcn_global_load_lds((const unsigned*)((const char*)Kbh + (size_t)(tile) * (64 * 384) + doffK[i]), (LAS unsigned*)(lds + (slot) * KT_BYTES + pc * 1024), 16, 0, 0); } } while (0)
; #define ATT_DMAV(tile, slot) do { _Pragma("unroll") for (int i = 0; i < 3; ++i) { const int pc = (wv + 8 * i) < 18 ? (wv + 8 * i) : 17; \
;         __builtin_amdgcn_global_load_lds((const unsigned*)((const char*)Vbh + (size_t)(tile) * 128 + doffV[i]), (LAS unsigned*)(lds + VRING + (slot) * VT_BYTES + pc * 1024), 16, 0, 0); } } while (0)
; #define ATT_SYNC(full) do { if (full) asm volatile("s_waitcnt vmcnt(7)" ::: "memory"); else asm volatile("s_waitcnt vmcnt(0)" ::: "memory"); \
;         __builtin_amdgcn_s_barrier(); asm volatile("" ::: "memory"); } while (0)
; __device__ __forceinline__ void attn_unit(const bf16_t* Qrows  , const bf16_t* Kbh, const bf16_t* Vbh, int nkeys, bf16_t* Orows, LAS unsigned char* lds) {
;     ...
;         k1 = k1 == 2 ? 0 : k1 + 1; v0 = v0 == 2 ? 0 : v0 + 1;
;         ATT_SYNC(j + 3 < nt);
;         if (j + 4 < nt) ATT_DMAK(j + 4, v0);
;         if (j + 3 < nt) ATT_DMAV(j + 3, v0 == 0 ? 2 : v0 - 1);
;         ATT_STEP(sB, sA, true, k1, v0);
;         k1 = k1 == 2 ? 0 : k1 + 1; v0 = v0 == 2 ? 0 : v0 + 1;
;     }
.LattB_end:
	s_add_i32 s13, s14, 1
	s_cmp_lg_u32 s14, 2
	s_cselect_b32 s14, s13, 0
	s_add_i32 s13, s12, 1
	s_cmp_lg_u32 s12, 2
	s_cselect_b32 s36, s13, 0
	s_add_u32 s80, s80, s6
	s_addc_u32 s81, s81, s7
	s_add_u32 s82, s82, s10
	s_addc_u32 s83, s83, s11
	s_add_i32 s63, s63, 2
	s_andn2_b64 vcc, exec, s[0:1]
	s_cbranch_vccz .LBB0_1250
.LBB0_1236:
	s_add_i32 s0, s63, -1
	s_cmp_lt_u32 s0, s64
	s_waitcnt vmcnt(7)
	s_barrier
	s_cselect_b64 s[24:25], -1, 0
	s_cmp_ge_u32 s0, s64
	s_cselect_b64 s[0:1], -1, 0
	s_mul_i32 s12, s36, 0x4800
	v_max_f32_e32 v82, v67, v67
	v_max_f32_e32 v83, v66, v66
	v_max_f32_e32 v82, v83, v82
	v_max3_f32 v82, v82, v68, v69
	v_max3_f32 v82, v82, v70, v71
	v_max3_f32 v82, v82, v72, v73
	v_max3_f32 v82, v82, v74, v75
	v_max3_f32 v82, v82, v76, v77
	v_max3_f32 v82, v82, v78, v79
	v_max3_f32 v82, v82, v80, v81
	v_mov_b32_e32 v83, v82
	s_nop 1
	v_permlane32_swap_b32_e32 v83, v82
	s_waitcnt lgkmcnt(0)
	v_max_f32_e32 v83, v83, v83
	v_max_f32_e32 v82, v82, v83
	v_add_f32_e32 v83, 0x41000000, v183
	v_cmp_gt_f32_e32 vcc, v82, v83
	s_cbranch_vccz .LBB0_1240
	v_max_f32_e32 v82, v82, v82
	v_max_f32_e32 v83, v183, v183
	v_max_f32_e32 v83, v83, v82
	v_sub_f32_e32 v82, v183, v83
	v_exp_f32_e32 v82, v82
	v_mov_b32_e32 v183, v83
	v_pk_mul_f32 v[64:65], v[64:65], v[82:83] op_sel_hi:[1,0]
	v_pk_mul_f32 v[62:63], v[62:63], v[82:83] op_sel_hi:[1,0]
	v_pk_mul_f32 v[60:61], v[60:61], v[82:83] op_sel_hi:[1,0]
	v_pk_mul_f32 v[58:59], v[58:59], v[82:83] op_sel_hi:[1,0]
	v_pk_mul_f32 v[56:57], v[56:57], v[82:83] op_sel_hi:[1,0]
	v_pk_mul_f32 v[54:55], v[54:55], v[82:83] op_sel_hi:[1,0]
	v_pk_mul_f32 v[52:53], v[52:53], v[82:83] op_sel_hi:[1,0]
	v_pk_mul_f32 v[50:51], v[50:51], v[82:83] op_sel_hi:[1,0]
	v_pk_mul_f32 v[48:49], v[48:49], v[82:83] op_sel_hi:[1,0]
	v_pk_mul_f32 v[46:47], v[46:47], v[82:83] op_sel_hi:[1,0]
	v_pk_mul_f32 v[44:45], v[44:45], v[82:83] op_sel_hi:[1,0]
	v_pk_mul_f32 v[42:43], v[42:43], v[82:83] op_sel_hi:[1,0]
	v_pk_mul_f32 v[40:41], v[40:41], v[82:83] op_sel_hi:[1,0]
	v_pk_mul_f32 v[38:39], v[38:39], v[82:83] op_sel_hi:[1,0]
	v_pk_mul_f32 v[36:37], v[36:37], v[82:83] op_sel_hi:[1,0]
	v_pk_mul_f32 v[34:35], v[34:35], v[82:83] op_sel_hi:[1,0]
	v_pk_mul_f32 v[32:33], v[32:33], v[82:83] op_sel_hi:[1,0]
	v_pk_mul_f32 v[30:31], v[30:31], v[82:83] op_sel_hi:[1,0]
	v_pk_mul_f32 v[28:29], v[28:29], v[82:83] op_sel_hi:[1,0]
	v_pk_mul_f32 v[26:27], v[26:27], v[82:83] op_sel_hi:[1,0]
	v_pk_mul_f32 v[24:25], v[24:25], v[82:83] op_sel_hi:[1,0]
	v_pk_mul_f32 v[22:23], v[22:23], v[82:83] op_sel_hi:[1,0]
	v_pk_mul_f32 v[20:21], v[20:21], v[82:83] op_sel_hi:[1,0]
	v_pk_mul_f32 v[18:19], v[18:19], v[82:83] op_sel_hi:[1,0]
	v_pk_mul_f32 v[16:17], v[16:17], v[82:83] op_sel_hi:[1,0]
	v_pk_mul_f32 v[14:15], v[14:15], v[82:83] op_sel_hi:[1,0]
	v_pk_mul_f32 v[12:13], v[12:13], v[82:83] op_sel_hi:[1,0]
	v_pk_mul_f32 v[10:11], v[10:11], v[82:83] op_sel_hi:[1,0]
	v_pk_mul_f32 v[8:9], v[8:9], v[82:83] op_sel_hi:[1,0]
	v_pk_mul_f32 v[6:7], v[6:7], v[82:83] op_sel_hi:[1,0]
	v_pk_mul_f32 v[4:5], v[4:5], v[82:83] op_sel_hi:[1,0]
	v_pk_mul_f32 v[2:3], v[2:3], v[82:83] op_sel_hi:[1,0]
	v_mul_f32_e32 v186, v186, v82
; #define ATT_DMAK(tile, slot) do { _Pragma("unroll") for (int i = 0; i < 4; ++i) { const int pc = (wv + 8 * i) < 25 ? (wv + 8 * i) : 24; \
;         __builtin_amdgcn_global_load_lds((const unsigned*)((const char*)Kbh + (size_t)(tile) * (64 * 384) + doffK[i]), (LAS unsigned*)(lds + (slot) * KT_BYTES + pc * 1024), 16, 0, 0); } } while (0)
; #define ATT_DMAV(tile, slot) do { _Pragma("unroll") for (int i = 0; i < 3; ++i) { const int pc = (wv + 8 * i) < 18 ? (wv + 8 * i) : 17; \
;         __builtin_amdgcn_global_load_lds((const unsigned*)((const char*)Vbh + (size_t)(tile) * 128 + doffV[i]), (LAS unsigned*)(lds + VRING + (slot) * VT_BYTES + pc * 1024), 16, 0, 0); } } while (0)
; __device__ __forceinline__ void attn_unit(const bf16_t* Qrows  , const bf16_t* Kbh, const bf16_t* Vbh, int nkeys, bf16_t* Orows, LAS unsigned char* lds) {
;     ...
;         if (j + 3 < nt) ATT_DMAK(j + 3, v0);
;         ATT_DMAV(j + 2, v0 == 0 ? 2 : v0 - 1);
.LBB0_1240:
	s_mul_i32 s13, s14, 0x6400
	v_add_u32_e32 v86, s13, v185
	ds_read_b128 v[82:85], v86
	ds_read_b128 v[188:191], v86 offset:32
	ds_read_b128 v[192:195], v86 offset:64
	ds_read_b128 v[196:199], v86 offset:96
	ds_read_b128 v[200:203], v86 offset:128
	ds_read_b128 v[216:219], v86 offset:160
	ds_read_b128 v[220:223], v86 offset:192
	ds_read_b128 v[224:227], v86 offset:224
	ds_read_b128 v[228:231], v86 offset:256
	ds_read_b128 v[232:235], v86 offset:288
	ds_read_b128 v[236:239], v86 offset:320
	ds_read_b128 v[240:243], v86 offset:352
	s_waitcnt lgkmcnt(11)
	v_mfma_f32_32x32x16_bf16 v[82:97], v[82:85], v[142:145], 0
	v_sub_f32_e32 v66, v66, v183
	v_sub_f32_e32 v78, v78, v183
	v_exp_f32_e32 v66, v66
	v_exp_f32_e32 v78, v78
	s_waitcnt lgkmcnt(10)
	v_mfma_f32_32x32x16_bf16 v[82:97], v[188:191], v[138:141], v[82:97]
	v_sub_f32_e32 v67, v67, v183
	v_sub_f32_e32 v79, v79, v183
	v_exp_f32_e32 v67, v67
	v_exp_f32_e32 v79, v79
	v_cvt_pk_bf16_f32 v188, v66, v67
	s_waitcnt lgkmcnt(9)
	v_mfma_f32_32x32x16_bf16 v[82:97], v[192:195], v[134:137], v[82:97]
	v_sub_f32_e32 v68, v68, v183
	v_sub_f32_e32 v80, v80, v183
	v_exp_f32_e32 v68, v68
	v_exp_f32_e32 v80, v80
	s_waitcnt lgkmcnt(8)
	v_mfma_f32_32x32x16_bf16 v[82:97], v[196:199], v[130:133], v[82:97]
	v_sub_f32_e32 v69, v69, v183
	v_sub_f32_e32 v81, v81, v183
	v_exp_f32_e32 v69, v69
	v_exp_f32_e32 v81, v81
	v_cvt_pk_bf16_f32 v194, v78, v79
	v_cvt_pk_bf16_f32 v189, v68, v69
	v_cvt_pk_bf16_f32 v195, v80, v81
	s_waitcnt lgkmcnt(7)
	v_mfma_f32_32x32x16_bf16 v[82:97], v[200:203], v[126:129], v[82:97]
	v_sub_f32_e32 v70, v70, v183
	v_exp_f32_e32 v70, v70
	s_waitcnt lgkmcnt(6)
	v_mfma_f32_32x32x16_bf16 v[82:97], v[216:219], v[122:125], v[82:97]
	v_sub_f32_e32 v71, v71, v183
	v_exp_f32_e32 v71, v71
	s_nop 0
	v_cvt_pk_bf16_f32 v190, v70, v71
	s_waitcnt lgkmcnt(5)
	v_mfma_f32_32x32x16_bf16 v[82:97], v[220:223], v[118:121], v[82:97]
	v_sub_f32_e32 v72, v72, v183
	v_exp_f32_e32 v72, v72
	s_waitcnt lgkmcnt(4)
	v_mfma_f32_32x32x16_bf16 v[82:97], v[224:227], v[114:117], v[82:97]
	v_sub_f32_e32 v73, v73, v183
	v_exp_f32_e32 v73, v73
	s_nop 0
	v_cvt_pk_bf16_f32 v191, v72, v73
	s_waitcnt lgkmcnt(3)
	v_mfma_f32_32x32x16_bf16 v[82:97], v[228:231], v[110:113], v[82:97]
	v_add_u32_e32 v204, s12, v187
	v_sub_f32_e32 v74, v74, v183
	ds_read_b128 v[196:199], v204
	ds_read_b128 v[200:203], v204 offset:32
	v_exp_f32_e32 v74, v74
	s_waitcnt lgkmcnt(4)
	v_mfma_f32_32x32x16_bf16 v[82:97], v[232:235], v[106:109], v[82:97]
	v_sub_f32_e32 v75, v75, v183
	ds_read_b128 v[216:219], v204 offset:4608
	ds_read_b128 v[220:223], v204 offset:4640
	v_exp_f32_e32 v75, v75
	s_nop 0
	v_cvt_pk_bf16_f32 v192, v74, v75
	s_waitcnt lgkmcnt(5)
	v_mfma_f32_32x32x16_bf16 v[82:97], v[236:239], v[102:105], v[82:97]
	v_sub_f32_e32 v76, v76, v183
	ds_read_b128 v[224:227], v204 offset:9216
	ds_read_b128 v[228:231], v204 offset:9248
	v_exp_f32_e32 v76, v76
	s_waitcnt lgkmcnt(6)
	v_mfma_f32_32x32x16_bf16 v[82:97], v[240:243], v[98:101], v[82:97]
	v_sub_f32_e32 v77, v77, v183
	ds_read_b128 v[232:235], v204 offset:13824
	ds_read_b128 v[236:239], v204 offset:13856
	v_exp_f32_e32 v77, v77
	s_nop 0
	v_cvt_pk_bf16_f32 v193, v76, v77
	s_waitcnt lgkmcnt(0)
	v_mfma_f32_32x32x16_bf16 v[50:65], v[196:199], v[188:191], v[50:65]
	v_mfma_f32_32x32x16_bf16 v[34:49], v[216:219], v[188:191], v[34:49]
	v_mfma_f32_32x32x16_bf16 v[18:33], v[224:227], v[188:191], v[18:33]
	v_mfma_f32_32x32x16_bf16 v[2:17], v[232:235], v[188:191], v[2:17]
	v_mfma_f32_32x32x16_bf16 v[50:65], v[200:203], v[192:195], v[50:65]
	v_mfma_f32_32x32x16_bf16 v[34:49], v[220:223], v[192:195], v[34:49]
	v_mfma_f32_32x32x16_bf16 v[18:33], v[228:231], v[192:195], v[18:33]
	v_mfma_f32_32x32x16_bf16 v[2:17], v[236:239], v[192:195], v[2:17]
	s_and_b64 vcc, exec, s[0:1]
	s_cbranch_vccnz .LattA_v
	s_mul_i32 s12, s36, 0x6400
	s_add_i32 s12, s12, 0
	s_add_u32 s16, s80, s2
	s_addc_u32 s17, s81, s3
	s_add_u32 s16, s16, 0x30e8a000
	s_addc_u32 s17, s17, 0
	s_add_i32 m0, s12, s65
	s_nop 0
	global_load_lds_dwordx4 v208, s[16:17]
	s_add_i32 m0, s12, s66
	s_nop 0
	global_load_lds_dwordx4 v209, s[16:17]
	s_add_i32 m0, s12, s67
	s_add_i32 s12, s12, s68
	global_load_lds_dwordx4 v210, s[16:17]
	s_add_i32 m0, s12, 0x6000
	s_nop 0
	global_load_lds_dwordx4 v211, s[16:17]
.LattA_v:
	s_mul_i32 s12, s36, 0x4800
	s_add_i32 s13, s12, 0xffffb800
	s_cmp_lg_u32 s36, 0
	s_cselect_b32 s13, s13, 0x9000
	s_add_i32 s13, s13, 0
	s_add_i32 s13, s13, 0x12c00
	s_add_u32 s16, s82, s2
	s_addc_u32 s17, s83, s3
	s_add_u32 s16, s16, s28
	s_addc_u32 s17, s17, s29
	s_add_i32 m0, s13, s69
	s_nop 0
	global_load_lds_dwordx4 v212, s[16:17]
	s_add_i32 m0, s13, s70
	s_nop 0
	global_load_lds_dwordx4 v213, s[16:17]
	s_add_i32 m0, s13, s71
	s_nop 0
	global_load_lds_dwordx4 v214, s[16:17]
	s_mov_b64 s[12:13], -1
	s_and_b64 vcc, exec, s[0:1]
	s_cbranch_vccz .LBB0_1242
	s_waitcnt vmcnt(0)
	s_mov_b64 s[12:13], 0

; #define ATT_DMAK(tile, slot) do { _Pragma("unroll") for (int i = 0; i < 4; ++i) { const int pc = (wv + 8 * i) < 25 ? (wv + 8 * i) : 24; \
;         __builtin_amdgcn_global_load_lds((const unsigned*)((const char*)Kbh + (size_t)(tile) * (64 * 384) + doffK[i]), (LAS unsigned*)(lds + (slot) * KT_BYTES + pc * 1024), 16, 0, 0); } } while (0)
; #define ATT_DMAV(tile, slot) do { _Pragma("unroll") for (int i = 0; i < 3; ++i) { const int pc = (wv + 8 * i) < 18 ? (wv + 8 * i) : 17; \
;         __builtin_amdgcn_global_load_lds((const unsigned*)((const char*)Vbh + (size_t)(tile) * 128 + doffV[i]), (LAS unsigned*)(lds + VRING + (slot) * VT_BYTES + pc * 1024), 16, 0, 0); } } while (0)
; #define ATT_SYNC(full) do { if (full) asm volatile("s_waitcnt vmcnt(7)" ::: "memory"); else asm volatile("s_waitcnt vmcnt(0)" ::: "memory"); \
;         __builtin_amdgcn_s_barrier(); asm volatile("" ::: "memory"); } while (0)
; __device__ __forceinline__ void attn_unit(const bf16_t* Qrows  , const bf16_t* Kbh, const bf16_t* Vbh, int nkeys, bf16_t* Orows, LAS unsigned char* lds) {
;     ...
;         k1 = k1 == 2 ? 0 : k1 + 1; v0 = v0 == 2 ? 0 : v0 + 1;
;         ATT_SYNC(j + 3 < nt);
;         if (j + 4 < nt) ATT_DMAK(j + 4, v0);
;         if (j + 3 < nt) ATT_DMAV(j + 3, v0 == 0 ? 2 : v0 - 1);
.LBB0_1244:
	s_add_i32 s0, s36, 1
	s_cmp_lg_u32 s36, 2
	s_cselect_b32 s12, s0, 0
	s_barrier
	s_cmp_ge_u32 s63, s64
	s_cselect_b64 s[0:1], -1, 0
	s_mul_i32 s13, s12, 0x4800
